# NA unit prologue: the full vmcnt drain before the first barrier relaxed to vmcnt(8) so the eight Q-fragment loads stay in flight (their counted waits already guard each use)
# speedup vs baseline: 1.0051x; 1.0051x over previous
.LBB0_1558:
	s_or_b64 exec, exec, s[6:7]
	v_cmp_gt_i32_e32 vcc, 64, v34
	s_and_saveexec_b64 s[6:7], vcc
	v_lshl_add_u32 v1, v34, 2, s43
	ds_write_b32 v1, v149 offset:2400
	s_or_b64 exec, exec, s[6:7]
	s_and_b32 s1, s0, 0x3fffffc0
	s_and_b32 s7, s86, 63
	s_lshl_b32 s1, s1, 2
	s_add_i32 s8, s1, 0
	s_lshl_b32 s1, s7, 2
	v_sub_u32_e64 v1, s1, 4 clamp
	s_ashr_i32 s9, s0, 6
	s_ashr_i32 s0, s0, 7
	v_readfirstlane_b32 s90, v1
	v_sub_u32_e64 v1, s1, 1 clamp
	s_add_i32 s0, s0, s1
	v_readfirstlane_b32 s1, v1
	s_min_u32 s92, s1, 0xf8
	s_max_i32 s10, s0, 4
	s_add_i32 s92, s92, 7
	s_lshl_b32 s16, s11, 7
	s_add_i32 s18, s10, -4
	s_sub_i32 s10, s92, s90
	s_ashr_i32 s17, s16, 31
	s_lshl_b32 s11, s9, 3
	v_bfe_u32 v1, v34, 4, 2
	v_bfe_u32 v2, v34, 2, 3
	v_lshrrev_b32_e32 v3, 1, v34
	s_lshl_b32 s19, s9, 2
	s_add_i32 s8, s8, 0x1e000
	s_lshl_b32 s6, s9, 5
	s_and_b32 s1, s10, -2
	v_bitop3_b32 v2, s11, v176, v2 bitop3:0xc8
	v_and_b32_e32 v3, 8, v3
	s_and_b32 s19, s19, 4
	v_or_b32_e32 v4, s11, v1
	v_bitop3_b32 v1, s11, v34, v1 bitop3:0x36
	s_movk_i32 s11, 0x1800
	s_min_u32 s87, s18, 0xf8
	s_lshl_b64 s[34:35], s[16:17], 1
	v_or3_b32 v2, v3, v2, s19
	v_lshlrev_b32_e32 v3, 3, v34
	v_mul_lo_u32 v5, v4, s11
	v_lshlrev_b32_e32 v1, 3, v1
	s_add_u32 s93, s29, s34
	v_and_b32_e32 v3, 24, v3
	v_mul_u32_u24_e32 v2, 0x1800, v2
	v_and_or_b32 v152, v1, s45, v5
	v_and_b32_e32 v1, 32, v34
	s_addc_u32 s94, s42, s35
	v_or3_b32 v154, v2, v3, v1
	s_add_u32 s38, s5, s34
	v_bitop3_b32 v1, v4, v34, 4 bitop3:0x36
	s_addc_u32 s39, s27, s35
	v_ashrrev_i32_e32 v155, 31, v154
	v_lshlrev_b32_e32 v1, 3, v1
	v_lshl_add_u64 v[2:3], v[154:155], 1, s[38:39]
	s_mov_b64 s[16:17], 0xc000000
	s_lshl_b32 s95, s9, 11
	v_and_or_b32 v1, v1, s45, v5
	v_lshl_add_u64 v[4:5], v[2:3], 0, s[16:17]
	s_mov_b64 s[16:17], 0xc000080
	s_or_b32 s96, s95, 0x400
	s_mov_b32 s9, m0
	s_mov_b32 m0, s95
	s_nop 0
	global_load_lds_dwordx4 v[4:5], off
	s_mov_b32 m0, s9
	v_lshl_add_u64 v[4:5], v[2:3], 0, s[16:17]
	s_add_u32 s16, s93, 0xc000000
	v_ashrrev_i32_e32 v153, 31, v152
	v_add_u32_e32 v156, 0x6000, v1
	s_mov_b32 s9, m0
	s_mov_b32 m0, s96
	s_nop 0
	global_load_lds_dwordx4 v[4:5], off
	s_mov_b32 m0, s9
	s_addc_u32 s17, s94, 0
	v_lshlrev_b64 v[4:5], 1, v[152:153]
	v_lshl_add_u64 v[6:7], s[16:17], 0, v[4:5]
	s_add_i32 s9, s95, 0x4000
	v_ashrrev_i32_e32 v157, 31, v156
	s_mov_b32 s11, m0
	s_mov_b32 m0, s9
	s_nop 0
	global_load_lds_dwordx4 v[6:7], off
	s_mov_b32 m0, s11
	v_lshlrev_b64 v[6:7], 1, v[156:157]
	s_add_i32 s9, s95, 0x4400
	v_lshl_add_u64 v[8:9], s[16:17], 0, v[6:7]
	s_mov_b32 s11, m0
	s_mov_b32 m0, s9
	s_nop 0
	global_load_lds_dwordx4 v[8:9], off
	s_mov_b32 m0, s11
	s_mov_b64 s[16:17], 0xc0c0000
	s_add_i32 s9, s95, 0x8000
	v_lshl_add_u64 v[8:9], v[2:3], 0, s[16:17]
	s_mov_b32 s11, m0
	s_mov_b32 m0, s9
	s_nop 0
	global_load_lds_dwordx4 v[8:9], off
	s_mov_b32 m0, s11
	s_mov_b64 s[16:17], 0xc0c0080
	s_add_i32 s9, s95, 0x8400
	v_lshl_add_u64 v[2:3], v[2:3], 0, s[16:17]
	s_add_u32 s16, s93, 0xc0c0000
	s_addc_u32 s17, s94, 0
	s_mov_b32 s11, m0
	s_mov_b32 m0, s9
	s_nop 0
	global_load_lds_dwordx4 v[2:3], off
	s_mov_b32 m0, s11
	v_lshl_add_u64 v[2:3], s[16:17], 0, v[4:5]
	s_lshl_b32 s7, s7, 8
	v_and_b32_e32 v179, 31, v34
	s_add_i32 s9, s95, 0xc000
	s_mov_b32 s11, m0
	s_mov_b32 m0, s9
	s_nop 0
	global_load_lds_dwordx4 v[2:3], off
	s_mov_b32 m0, s11
	v_lshl_add_u64 v[2:3], s[16:17], 0, v[6:7]
	s_add_i32 s36, s6, s7
	s_add_i32 s9, s95, 0xc400
	s_mov_b32 s11, m0
	s_mov_b32 m0, s9
	s_nop 0
	global_load_lds_dwordx4 v[2:3], off
	s_mov_b32 m0, s11
	v_or_b32_e32 v1, s36, v179
	v_mov_b64_e32 v[2:3], s[24:25]
	v_bfe_u32 v178, v34, 5, 1
	v_mad_i64_i32 v[2:3], s[16:17], v1, s46, v[2:3]
	v_lshl_add_u64 v[2:3], v[2:3], 0, s[34:35]
	v_lshlrev_b32_e32 v148, 4, v178
	v_lshl_add_u64 v[2:3], v[2:3], 0, v[148:149]
	global_load_dwordx4 v[136:139], v[2:3], off
	global_load_dwordx4 v[132:135], v[2:3], off offset:32
	global_load_dwordx4 v[128:131], v[2:3], off offset:64
	global_load_dwordx4 v[124:127], v[2:3], off offset:96
	global_load_dwordx4 v[120:123], v[2:3], off offset:128
	global_load_dwordx4 v[116:119], v[2:3], off offset:160
	global_load_dwordx4 v[112:115], v[2:3], off offset:192
	global_load_dwordx4 v[108:111], v[2:3], off offset:224
	v_lshlrev_b32_e32 v35, 4, v34
	v_lshlrev_b32_e32 v191, 8, v179
	s_movk_i32 s7, 0xf0
	v_add_u32_e32 v194, 0, v191
	v_bitop3_b32 v192, v148, v35, s7 bitop3:0x78
	s_waitcnt vmcnt(8) lgkmcnt(0)
	s_barrier
	v_add_u32_e32 v1, v194, v192
	ds_read_b128 v[2:5], v1 offset:16384
	ds_read_b128 v[6:9], v1 offset:24576
	s_waitcnt vmcnt(7) lgkmcnt(1)
	v_mfma_f32_32x32x16_bf16 v[18:33], v[2:5], v[136:139], 0
	v_and_b32_e32 v44, 0xf0, v35
	v_bitop3_b32 v193, v148, v44, 32 bitop3:0x36
	v_add_u32_e32 v1, v194, v193
	ds_read_b128 v[36:39], v1 offset:16384
	ds_read_b128 v[40:43], v1 offset:24576
	v_bitop3_b32 v187, v148, v44, 64 bitop3:0x36
	v_add_u32_e32 v1, v194, v187
	s_movk_i32 s7, 0x60
	s_waitcnt lgkmcnt(2)
	v_mfma_f32_32x32x16_bf16 v[2:17], v[6:9], v[136:139], 0
	v_bitop3_b32 v186, v148, v44, s7 bitop3:0x36
	s_movk_i32 s7, 0x80
	v_bitop3_b32 v189, v148, v44, s7 bitop3:0x36
	s_movk_i32 s7, 0xa0
	v_bitop3_b32 v190, v148, v44, s7 bitop3:0x36
	s_movk_i32 s7, 0xc0
	v_bitop3_b32 v185, v148, v44, s7 bitop3:0x36
	s_waitcnt vmcnt(6) lgkmcnt(1)
	v_mfma_f32_32x32x16_bf16 v[18:33], v[36:39], v[132:135], v[18:33]
	v_and_or_b32 v45, s6, 32, v179
	s_movk_i32 s6, 0xe0
	v_bitop3_b32 v188, v148, v44, s6 bitop3:0x36
	v_add_u32_e32 v44, v194, v188
	s_mov_b64 s[6:7], 0xffff
	v_and_b32_e32 v180, 63, v34
	v_and_b32_e32 v35, 0xc0, v35
	s_waitcnt lgkmcnt(0)
	v_mfma_f32_32x32x16_bf16 v[2:17], v[40:43], v[132:135], v[2:17]
	ds_read_b128 v[36:39], v1 offset:16384
	ds_read_b128 v[40:43], v1 offset:24576
	v_add_u32_e32 v1, v194, v186
	v_lshlrev_b32_e32 v34, 1, v34
	v_and_b32_e32 v34, 32, v34
	s_mov_b32 s89, 0x8000
	s_mov_b32 s91, 0
	s_add_i32 s88, s87, 8
	s_waitcnt vmcnt(5) lgkmcnt(1)
	v_mfma_f32_32x32x16_bf16 v[18:33], v[36:39], v[128:131], v[18:33]
	s_waitcnt lgkmcnt(0)
	v_mfma_f32_32x32x16_bf16 v[2:17], v[40:43], v[128:131], v[2:17]
	ds_read_b128 v[36:39], v1 offset:16384
	ds_read_b128 v[40:43], v1 offset:24576
	v_add_u32_e32 v1, v194, v189
	s_waitcnt vmcnt(4) lgkmcnt(1)
	v_mfma_f32_32x32x16_bf16 v[18:33], v[36:39], v[124:127], v[18:33]
	s_waitcnt lgkmcnt(0)
	v_mfma_f32_32x32x16_bf16 v[2:17], v[40:43], v[124:127], v[2:17]
	ds_read_b128 v[36:39], v1 offset:16384
	ds_read_b128 v[40:43], v1 offset:24576
	v_add_u32_e32 v1, v194, v190
	s_waitcnt vmcnt(3) lgkmcnt(1)
	v_mfma_f32_32x32x16_bf16 v[18:33], v[36:39], v[120:123], v[18:33]
	s_waitcnt lgkmcnt(0)
	v_mfma_f32_32x32x16_bf16 v[2:17], v[40:43], v[120:123], v[2:17]
	ds_read_b128 v[36:39], v1 offset:16384
	ds_read_b128 v[40:43], v1 offset:24576
	v_add_u32_e32 v1, v194, v185
	s_waitcnt vmcnt(2) lgkmcnt(1)
	v_mfma_f32_32x32x16_bf16 v[18:33], v[36:39], v[116:119], v[18:33]
	ds_read_b128 v[36:39], v1 offset:16384
	s_waitcnt lgkmcnt(1)
	v_mfma_f32_32x32x16_bf16 v[2:17], v[40:43], v[116:119], v[2:17]
	ds_read_b128 v[40:43], v1 offset:24576
	v_sub_u32_e64 v1, v45, 8 clamp
	v_min_u32_e32 v46, 48, v1
	v_lshlrev_b32_e32 v1, 2, v178
	v_sub_u32_e32 v183, v1, v45
	v_lshlrev_b32_e32 v45, 3, v180
	v_and_or_b32 v35, v45, 24, v35
	s_waitcnt vmcnt(1) lgkmcnt(1)
	v_mfma_f32_32x32x16_bf16 v[18:33], v[36:39], v[112:115], v[18:33]
	ds_read_b128 v[36:39], v44 offset:16384
	s_waitcnt lgkmcnt(1)
	v_mfma_f32_32x32x16_bf16 v[2:17], v[40:43], v[112:115], v[2:17]
	v_lshlrev_b64 v[40:41], v46, s[6:7]
	v_lshrrev_b64 v[150:151], v1, v[40:41]
	v_lshrrev_b32_e32 v184, v1, v41
	ds_read_b128 v[40:43], v44 offset:24576
	s_waitcnt vmcnt(0) lgkmcnt(1)
	v_mfma_f32_32x32x16_bf16 v[18:33], v[36:39], v[108:111], v[18:33]
	v_and_b32_e32 v36, 0x100, v45
	v_or3_b32 v148, v35, v34, v36
	v_mov_b32_e32 v34, s47
	v_mov_b32_e32 v35, s48
	v_mov_b32_e32 v36, s49
	v_mov_b32_e32 v37, s50
	v_mov_b32_e32 v38, s51
	s_waitcnt lgkmcnt(0)
	v_mfma_f32_32x32x16_bf16 v[2:17], v[40:43], v[108:111], v[2:17]
	v_mov_b32_e32 v39, s52
	v_mov_b32_e32 v40, s53
	v_mov_b32_e32 v41, s54
	ds_read_b32 v34, v34
	ds_read_b32 v35, v35
	ds_read_b32 v36, v36
	ds_read_b32 v37, v37
	ds_read_b32 v38, v38
	ds_read_b32 v39, v39
	ds_read_b32 v40, v40
	ds_read_b32 v41, v41
	s_waitcnt lgkmcnt(7)
	v_bfi_b32 v34, v174, v34, v175
	s_waitcnt lgkmcnt(6)
	v_bfi_b32 v35, v174, v35, v175
	s_nop 0
	v_pk_fma_f32 v[18:19], v[18:19], s[28:29], v[34:35] op_sel_hi:[1,0,1]
	s_waitcnt lgkmcnt(5)
	v_bfi_b32 v34, v174, v36, v175
	s_waitcnt lgkmcnt(4)
	v_bfi_b32 v35, v174, v37, v175
	s_nop 0
	v_pk_fma_f32 v[20:21], v[20:21], s[28:29], v[34:35] op_sel_hi:[1,0,1]
	s_waitcnt lgkmcnt(3)
	v_bfi_b32 v34, v174, v38, v175
	s_waitcnt lgkmcnt(2)
	v_bfi_b32 v35, v174, v39, v175
	s_nop 0
	v_pk_fma_f32 v[22:23], v[22:23], s[28:29], v[34:35] op_sel_hi:[1,0,1]
	s_waitcnt lgkmcnt(1)
	v_bfi_b32 v34, v174, v40, v175
	s_waitcnt lgkmcnt(0)
	v_bfi_b32 v35, v174, v41, v175
	s_nop 0
	v_pk_fma_f32 v[24:25], v[24:25], s[28:29], v[34:35] op_sel_hi:[1,0,1]
	v_mov_b32_e32 v34, s55
	v_mov_b32_e32 v35, s56
	v_mov_b32_e32 v36, s57
	v_mov_b32_e32 v37, s58
	v_mov_b32_e32 v38, s59
	v_mov_b32_e32 v39, s61
	v_mov_b32_e32 v40, s66
	v_mov_b32_e32 v41, s67
	ds_read_b32 v34, v34
	ds_read_b32 v35, v35
	ds_read_b32 v36, v36
	ds_read_b32 v37, v37
	ds_read_b32 v38, v38
	ds_read_b32 v39, v39
	ds_read_b32 v40, v40
	ds_read_b32 v41, v41
	s_waitcnt lgkmcnt(7)
	v_bfi_b32 v34, v174, v34, v175
	s_waitcnt lgkmcnt(6)
	v_bfi_b32 v35, v174, v35, v175
	s_nop 0
	v_pk_fma_f32 v[26:27], v[26:27], s[28:29], v[34:35] op_sel_hi:[1,0,1]
	s_waitcnt lgkmcnt(5)
	v_bfi_b32 v34, v174, v36, v175
	s_waitcnt lgkmcnt(4)
	v_bfi_b32 v35, v174, v37, v175
	s_nop 0
	v_pk_fma_f32 v[28:29], v[28:29], s[28:29], v[34:35] op_sel_hi:[1,0,1]
	s_waitcnt lgkmcnt(3)
	v_bfi_b32 v34, v174, v38, v175
	s_waitcnt lgkmcnt(2)
	v_bfi_b32 v35, v174, v39, v175
	s_nop 0
	v_pk_fma_f32 v[30:31], v[30:31], s[28:29], v[34:35] op_sel_hi:[1,0,1]
	s_waitcnt lgkmcnt(1)
	v_bfi_b32 v34, v174, v40, v175
	s_waitcnt lgkmcnt(0)
	v_bfi_b32 v35, v174, v41, v175
	s_nop 0
	v_pk_fma_f32 v[32:33], v[32:33], s[28:29], v[34:35] op_sel_hi:[1,0,1]
	v_mov_b32_e32 v34, s68
	v_mov_b32_e32 v35, s69
	v_mov_b32_e32 v36, s70
	v_mov_b32_e32 v37, s71
	v_mov_b32_e32 v38, s72
	v_mov_b32_e32 v39, s73
	v_mov_b32_e32 v40, s74
	v_mov_b32_e32 v41, s75
	ds_read_b32 v34, v34
	ds_read_b32 v35, v35
	ds_read_b32 v36, v36
	ds_read_b32 v37, v37
	ds_read_b32 v38, v38
	ds_read_b32 v39, v39
	ds_read_b32 v40, v40
	ds_read_b32 v41, v41
	s_waitcnt lgkmcnt(7)
	v_bfi_b32 v34, v174, v34, v175
	s_waitcnt lgkmcnt(6)
	v_bfi_b32 v35, v174, v35, v175
	s_nop 0
	v_pk_fma_f32 v[2:3], v[2:3], s[28:29], v[34:35] op_sel_hi:[1,0,1]
	s_waitcnt lgkmcnt(5)
	v_bfi_b32 v34, v174, v36, v175
	s_waitcnt lgkmcnt(4)
	v_bfi_b32 v35, v174, v37, v175
	s_nop 0
	v_pk_fma_f32 v[4:5], v[4:5], s[28:29], v[34:35] op_sel_hi:[1,0,1]
	s_waitcnt lgkmcnt(3)
	v_bfi_b32 v34, v174, v38, v175
	s_waitcnt lgkmcnt(2)
	v_bfi_b32 v35, v174, v39, v175
	s_nop 0
	v_pk_fma_f32 v[6:7], v[6:7], s[28:29], v[34:35] op_sel_hi:[1,0,1]
	s_waitcnt lgkmcnt(1)
	v_bfi_b32 v34, v174, v40, v175
	s_waitcnt lgkmcnt(0)
	v_bfi_b32 v35, v174, v41, v175
	s_nop 0
	v_pk_fma_f32 v[8:9], v[8:9], s[28:29], v[34:35] op_sel_hi:[1,0,1]
	v_mov_b32_e32 v34, s76
	v_mov_b32_e32 v35, s77
	v_mov_b32_e32 v36, s78
	v_mov_b32_e32 v37, s79
	v_mov_b32_e32 v38, s80
	v_mov_b32_e32 v39, s81
	v_mov_b32_e32 v40, s82
	v_mov_b32_e32 v41, s83
	ds_read_b32 v34, v34
	ds_read_b32 v35, v35
	ds_read_b32 v36, v36
	ds_read_b32 v37, v37
	ds_read_b32 v38, v38
	ds_read_b32 v39, v39
	ds_read_b32 v40, v40
	ds_read_b32 v41, v41
	s_waitcnt lgkmcnt(7)
	v_bfi_b32 v34, v174, v34, v175
	s_waitcnt lgkmcnt(6)
	v_bfi_b32 v35, v174, v35, v175
	s_nop 0
	v_pk_fma_f32 v[10:11], v[10:11], s[28:29], v[34:35] op_sel_hi:[1,0,1]
	s_waitcnt lgkmcnt(5)
	v_bfi_b32 v34, v174, v36, v175
	s_waitcnt lgkmcnt(4)
	v_bfi_b32 v35, v174, v37, v175
	s_nop 0
	v_pk_fma_f32 v[12:13], v[12:13], s[28:29], v[34:35] op_sel_hi:[1,0,1]
	s_waitcnt lgkmcnt(3)
	v_bfi_b32 v34, v174, v38, v175
	s_waitcnt lgkmcnt(2)
	v_bfi_b32 v35, v174, v39, v175
	s_nop 0
	v_pk_fma_f32 v[14:15], v[14:15], s[28:29], v[34:35] op_sel_hi:[1,0,1]
	s_waitcnt lgkmcnt(1)
	v_bfi_b32 v34, v174, v40, v175
	s_waitcnt lgkmcnt(0)
	v_bfi_b32 v35, v174, v41, v175
	s_nop 0
	v_pk_fma_f32 v[16:17], v[16:17], s[28:29], v[34:35] op_sel_hi:[1,0,1]
	v_max_f32_e32 v34, v18, v19
	v_max3_f32 v34, v34, v20, v21
	v_max3_f32 v34, v34, v22, v23
	v_max3_f32 v34, v34, v24, v25
	v_max3_f32 v34, v34, v26, v27
	v_max3_f32 v34, v34, v28, v29
	v_max3_f32 v34, v34, v30, v31
	v_max3_f32 v34, v34, v32, v33
	v_max3_f32 v34, v34, v2, v3
	v_max3_f32 v34, v34, v4, v5
	v_max3_f32 v34, v34, v6, v7
	v_max3_f32 v34, v34, v8, v9
	v_max3_f32 v34, v34, v10, v11
	v_max3_f32 v34, v34, v12, v13
	v_max3_f32 v34, v34, v14, v15
	v_max3_f32 v34, v34, v16, v17
	v_mov_b32_e32 v35, v34
	s_nop 1
	v_permlane32_swap_b32_e32 v34, v35
	v_max_f32_e32 v35, v35, v35
	v_max_f32_e32 v34, v34, v34
	v_max_f32_e32 v34, v34, v35
	v_add_f32_e32 v35, 0x7149f2ca, v34
	v_cmp_ge_f32_e32 vcc, s84, v35
	s_cmp_eq_u64 vcc, exec
	v_max_f32_e32 v34, 0xf149f2ca, v34
	s_cselect_b64 vcc, -1, 0
	v_sub_f32_e32 v35, 0xf149f2ca, v34
	v_cndmask_b32_e32 v198, v34, v177, vcc
	v_exp_f32_e32 v35, v35
	v_sub_f32_e32 v33, v33, v198
	v_sub_f32_e32 v32, v32, v198
	v_sub_f32_e32 v31, v31, v198
	v_sub_f32_e32 v30, v30, v198
	v_sub_f32_e32 v29, v29, v198
	v_sub_f32_e32 v28, v28, v198
	v_sub_f32_e32 v27, v27, v198
	v_sub_f32_e32 v26, v26, v198
	v_sub_f32_e32 v25, v25, v198
	v_sub_f32_e32 v24, v24, v198
	v_sub_f32_e32 v23, v23, v198
	v_sub_f32_e32 v22, v22, v198
	v_sub_f32_e32 v21, v21, v198
	v_sub_f32_e32 v20, v20, v198
	v_sub_f32_e32 v19, v19, v198
	v_sub_f32_e32 v18, v18, v198
	v_exp_f32_e32 v166, v18
	v_exp_f32_e32 v167, v19
	v_exp_f32_e32 v164, v20
	v_exp_f32_e32 v165, v21
	v_exp_f32_e32 v162, v22
	v_exp_f32_e32 v163, v23
	v_exp_f32_e32 v160, v24
	v_exp_f32_e32 v161, v25
	v_exp_f32_e32 v146, v26
	v_exp_f32_e32 v147, v27
	v_exp_f32_e32 v144, v28
	v_exp_f32_e32 v145, v29
	v_exp_f32_e32 v142, v30
	v_exp_f32_e32 v143, v31
	v_exp_f32_e32 v140, v32
	v_exp_f32_e32 v141, v33
	s_add_i32 s97, s1, 5
	v_cndmask_b32_e64 v195, v35, 1.0, vcc
	v_sub_f32_e32 v67, v17, v198
	v_sub_f32_e32 v66, v16, v198
	v_sub_f32_e32 v69, v15, v198
	v_sub_f32_e32 v68, v14, v198
	v_sub_f32_e32 v71, v13, v198
	s_cmp_lt_i32 s1, -3
	v_cmp_gt_u32_e64 s[6:7], 32, v180
	v_lshl_add_u32 v181, v179, 2, s8
	v_lshl_add_u32 v151, v1, 2, s8
	v_sub_f32_e32 v70, v12, v198
	v_sub_f32_e32 v73, v11, v198
	v_sub_f32_e32 v72, v10, v198
	v_sub_f32_e32 v75, v9, v198
	v_sub_f32_e32 v74, v8, v198
	v_sub_f32_e32 v77, v7, v198
	v_sub_f32_e32 v76, v6, v198
	v_sub_f32_e32 v79, v5, v198
	v_sub_f32_e32 v78, v4, v198
	v_sub_f32_e32 v1, v3, v198
	v_sub_f32_e32 v80, v2, v198
	v_mov_b32_e32 v17, 0
	s_cbranch_scc1 .LBB0_1586
	s_and_b32 s8, s85, 63
	s_lshl_b32 s8, s8, 2
	s_min_u32 s9, s8, 4
	v_mov_b32_e32 v182, 0
	s_add_i32 s37, s10, 4
	s_add_i32 s44, s10, 3
	s_sub_i32 s11, s8, s9
	s_mov_b32 s33, 2
	v_lshl_add_u32 v196, v183, 2, s43
	s_mov_b32 s64, 1
	s_mov_b32 s8, 0
	s_movk_i32 s65, 0x4080
	s_mov_b32 s16, 1
	v_mov_b32_e32 v50, 0
	v_mov_b32_e32 v51, v182
	v_mov_b32_e32 v52, v182
	v_mov_b32_e32 v53, v182
	v_mov_b32_e32 v54, v182
	v_mov_b32_e32 v55, v182
	v_mov_b32_e32 v56, v182
	v_mov_b32_e32 v57, v182
	v_mov_b32_e32 v58, v182
	v_mov_b32_e32 v59, v182
	v_mov_b32_e32 v60, v182
	v_mov_b32_e32 v61, v182
	v_mov_b32_e32 v62, v182
	v_mov_b32_e32 v63, v182
	v_mov_b32_e32 v64, v182
	v_mov_b32_e32 v65, v182
	v_mov_b32_e32 v34, 0
	v_mov_b32_e32 v35, v182
	v_mov_b32_e32 v36, v182
	v_mov_b32_e32 v37, v182
	v_mov_b32_e32 v38, v182
	v_mov_b32_e32 v39, v182
	v_mov_b32_e32 v40, v182
	v_mov_b32_e32 v41, v182
	v_mov_b32_e32 v42, v182
	v_mov_b32_e32 v43, v182
	v_mov_b32_e32 v44, v182
	v_mov_b32_e32 v45, v182
	v_mov_b32_e32 v46, v182
	v_mov_b32_e32 v47, v182
	v_mov_b32_e32 v48, v182
	v_mov_b32_e32 v49, v182
	v_mov_b32_e32 v18, 0
	v_mov_b32_e32 v19, v182
	v_mov_b32_e32 v20, v182
	v_mov_b32_e32 v21, v182
	v_mov_b32_e32 v22, v182
	v_mov_b32_e32 v23, v182
	v_mov_b32_e32 v24, v182
	v_mov_b32_e32 v25, v182
	v_mov_b32_e32 v26, v182
	v_mov_b32_e32 v27, v182
	v_mov_b32_e32 v28, v182
	v_mov_b32_e32 v29, v182
	v_mov_b32_e32 v30, v182
	v_mov_b32_e32 v31, v182
	v_mov_b32_e32 v32, v182
	v_mov_b32_e32 v33, v182
	v_mov_b32_e32 v2, 0
	v_mov_b32_e32 v3, v182
	v_mov_b32_e32 v4, v182
	v_mov_b32_e32 v5, v182
	v_mov_b32_e32 v6, v182
	v_mov_b32_e32 v7, v182
	v_mov_b32_e32 v8, v182
	v_mov_b32_e32 v9, v182
	v_mov_b32_e32 v10, v182
	v_mov_b32_e32 v11, v182
	v_mov_b32_e32 v12, v182
	v_mov_b32_e32 v13, v182
	v_mov_b32_e32 v14, v182
	v_mov_b32_e32 v15, v182
	v_mov_b32_e32 v16, v182
	v_mov_b32_e32 v17, v182
